# down GEMM: slot-list entries (dest row, gate) of each unit requested at the unit top instead of in the epilogue; waits that counted loads past younger stores made full drains again (gate/up bias wait,
# baseline (speedup 1.0000x reference)
;     __device__ __forceinline__ void init(f32x4 (&acc)[2][2][4][2], const Pre& p) const {
; #pragma unroll
;         for (int bj = 0; bj < 2; ++bj)
; #pragma unroll
;             for (int a = 0; a < 2; ++a)
; #pragma unroll
;                 for (int m = 0; m < 4; ++m) { acc[a][bj][m][0] = p.v[2 * bj]; acc[a][bj][m][1] = p.v[2 * bj + 1]; } }
;     __device__ __forceinline__ void operator()(const f32x4 (&acc)[2][2][4][2], const Unit& u, int wr, int wc, int fr, int fq) const {
;     ...
;         int2 sr[2][4];
; #pragma unroll
;         for (int ai = 0; ai < 2; ++ai)
; #pragma unroll
;             for (int m = 0; m < 4; ++m) { const int rl = rl0 + ai * HALF + m * 16;
;                 sr[ai][m] = SLOT[(size_t)u.aux * GCAP_SLOTS + (size_t)u.lt * BM + (rl < u.rows ? rl : 0)]; }
.LBB0_1173:
	s_ashr_i32 s29, s28, 31
	s_lshl_b64 s[14:15], s[28:29], 19
	s_add_u32 s34, s0, s14
	s_addc_u32 s35, s38, s15
	s_and_b64 s[14:15], s[30:31], exec
	s_cselect_b32 s7, s35, s13
	s_cselect_b32 s9, s34, s12
	s_ashr_i32 s27, s26, 31
	s_lshl_b64 s[14:15], s[26:27], 19
	s_add_u32 s36, s39, s14
	s_addc_u32 s37, s42, s15
	s_and_b64 s[14:15], s[30:31], exec
	s_cselect_b32 s18, s37, s11
	s_cselect_b32 s19, s36, s10
	s_add_u32 s12, s12, 0x40080
	s_addc_u32 s13, s13, 0
	s_add_u32 s27, s10, 0x100
	s_waitcnt vmcnt(16)
	v_mov_b64_e32 v[20:21], v[4:5]
	v_mov_b64_e32 v[24:25], v[8:9]
	v_mov_b64_e32 v[36:37], v[4:5]
	v_mov_b64_e32 v[40:41], v[8:9]
	v_mov_b64_e32 v[52:53], v[4:5]
	v_mov_b64_e32 v[56:57], v[8:9]
	v_mov_b64_e32 v[28:29], v[12:13]
	v_mov_b64_e32 v[32:33], v[16:17]
	v_mov_b64_e32 v[44:45], v[12:13]
	v_mov_b64_e32 v[48:49], v[16:17]
	v_mov_b64_e32 v[60:61], v[12:13]
	v_mov_b64_e32 v[64:65], v[16:17]
	v_mov_b64_e32 v[84:85], v[4:5]
	v_mov_b64_e32 v[88:89], v[8:9]
	v_mov_b64_e32 v[100:101], v[4:5]
	v_mov_b64_e32 v[104:105], v[8:9]
	v_mov_b64_e32 v[116:117], v[4:5]
	v_mov_b64_e32 v[120:121], v[8:9]
	v_mov_b64_e32 v[132:133], v[4:5]
	v_mov_b64_e32 v[136:137], v[8:9]
	v_mov_b64_e32 v[92:93], v[12:13]
	v_mov_b64_e32 v[96:97], v[16:17]
	v_mov_b64_e32 v[108:109], v[12:13]
	v_mov_b64_e32 v[112:113], v[16:17]
	v_mov_b64_e32 v[124:125], v[12:13]
	v_mov_b64_e32 v[128:129], v[16:17]
	v_mov_b64_e32 v[140:141], v[12:13]
	v_mov_b64_e32 v[144:145], v[16:17]
	s_addc_u32 s29, s11, 0
	s_mov_b32 s67, -2
	v_mov_b64_e32 v[18:19], v[2:3]
	v_mov_b64_e32 v[22:23], v[6:7]
	v_mov_b64_e32 v[34:35], v[2:3]
	v_mov_b64_e32 v[38:39], v[6:7]
	v_mov_b64_e32 v[50:51], v[2:3]
	v_mov_b64_e32 v[54:55], v[6:7]
	v_mov_b64_e32 v[26:27], v[10:11]
	v_mov_b64_e32 v[30:31], v[14:15]
	v_mov_b64_e32 v[42:43], v[10:11]
	v_mov_b64_e32 v[46:47], v[14:15]
	v_mov_b64_e32 v[58:59], v[10:11]
	v_mov_b64_e32 v[62:63], v[14:15]
	v_mov_b64_e32 v[82:83], v[2:3]
	v_mov_b64_e32 v[86:87], v[6:7]
	v_mov_b64_e32 v[98:99], v[2:3]
	v_mov_b64_e32 v[102:103], v[6:7]
	v_mov_b64_e32 v[114:115], v[2:3]
	v_mov_b64_e32 v[118:119], v[6:7]
	v_mov_b64_e32 v[130:131], v[2:3]
	v_mov_b64_e32 v[134:135], v[6:7]
	v_mov_b64_e32 v[90:91], v[10:11]
	v_mov_b64_e32 v[94:95], v[14:15]
	v_mov_b64_e32 v[106:107], v[10:11]
	v_mov_b64_e32 v[110:111], v[14:15]
	v_mov_b64_e32 v[122:123], v[10:11]
	v_mov_b64_e32 v[126:127], v[14:15]
	v_mov_b64_e32 v[138:139], v[10:11]
	v_mov_b64_e32 v[142:143], v[14:15]
	s_lshl_b32 s68, s4, 18
	s_lshl_b32 s69, s6, 11
	s_add_i32 s68, s68, s69
	s_add_u32 s68, s53, s68
	s_addc_u32 s69, s56, 0
	v_mov_b32_e32 v220, v167
	v_cmp_gt_i32_e32 vcc, s65, v220
	s_nop 1
	v_cndmask_b32_e32 v220, 0, v220, vcc
	v_ashrrev_i32_e32 v221, 31, v220
	v_lshl_add_u64 v[220:221], v[220:221], 3, s[68:69]
	global_load_dwordx2 v[220:221], v[220:221], off
	v_add_u32_e32 v222, 0x10, v167
	v_cmp_gt_i32_e32 vcc, s65, v222
	s_nop 1
	v_cndmask_b32_e32 v222, 0, v222, vcc
	v_ashrrev_i32_e32 v223, 31, v222
	v_lshl_add_u64 v[222:223], v[222:223], 3, s[68:69]
	global_load_dwordx2 v[222:223], v[222:223], off
	v_add_u32_e32 v224, 0x20, v167
	v_cmp_gt_i32_e32 vcc, s65, v224
	s_nop 1
	v_cndmask_b32_e32 v224, 0, v224, vcc
	v_ashrrev_i32_e32 v225, 31, v224
	v_lshl_add_u64 v[224:225], v[224:225], 3, s[68:69]
	global_load_dwordx2 v[224:225], v[224:225], off
	v_add_u32_e32 v226, 0x30, v167
	v_cmp_gt_i32_e32 vcc, s65, v226
	s_nop 1
	v_cndmask_b32_e32 v226, 0, v226, vcc
	v_ashrrev_i32_e32 v227, 31, v226
	v_lshl_add_u64 v[226:227], v[226:227], 3, s[68:69]
	global_load_dwordx2 v[226:227], v[226:227], off
	v_add_u32_e32 v240, 0x80, v167
	v_cmp_gt_i32_e32 vcc, s65, v240
	s_nop 1
	v_cndmask_b32_e32 v240, 0, v240, vcc
	v_ashrrev_i32_e32 v241, 31, v240
	v_lshl_add_u64 v[240:241], v[240:241], 3, s[68:69]
	global_load_dwordx2 v[240:241], v[240:241], off
	v_add_u32_e32 v242, 0x90, v167
	v_cmp_gt_i32_e32 vcc, s65, v242
	s_nop 1
	v_cndmask_b32_e32 v242, 0, v242, vcc
	v_ashrrev_i32_e32 v243, 31, v242
	v_lshl_add_u64 v[242:243], v[242:243], 3, s[68:69]
	global_load_dwordx2 v[242:243], v[242:243], off
	v_add_u32_e32 v244, 0xa0, v167
	v_cmp_gt_i32_e32 vcc, s65, v244
	s_nop 1
	v_cndmask_b32_e32 v244, 0, v244, vcc
	v_ashrrev_i32_e32 v245, 31, v244
	v_lshl_add_u64 v[244:245], v[244:245], 3, s[68:69]
	global_load_dwordx2 v[244:245], v[244:245], off
	v_add_u32_e32 v246, 0xb0, v167
	v_cmp_gt_i32_e32 vcc, s65, v246
	s_nop 1
	v_cndmask_b32_e32 v246, 0, v246, vcc
	v_ashrrev_i32_e32 v247, 31, v246
	v_lshl_add_u64 v[246:247], v[246:247], 3, s[68:69]
	global_load_dwordx2 v[246:247], v[246:247], off

; __device__ __forceinline__ u32x4 pack8(const f32x4 v0, const f32x4 v1) { u32x4 w; w.x = cvt_pk_bf16(v0[0], v0[1]); w.y = cvt_pk_bf16(v0[2], v0[3]); w.z = cvt_pk_bf16(v1[0], v1[1]); w.w = cvt_pk_bf16(v1[2], v1[3]); return w; }
;     __device__ __forceinline__ void init(f32x4 (&acc)[2][2][4][2], const Pre& p) const {
; #pragma unroll
;         for (int bj = 0; bj < 2; ++bj)
; #pragma unroll
;             for (int a = 0; a < 2; ++a)
; #pragma unroll
;                 for (int m = 0; m < 4; ++m) { acc[a][bj][m][0] = p.v[2 * bj]; acc[a][bj][m][1] = p.v[2 * bj + 1]; } }
;     __device__ __forceinline__ void operator()(const f32x4 (&acc)[2][2][4][2], const Unit& u, int wr, int wc, int fr, int fq) const {
;         int rl0 = wr * 64 + fr; asm volatile("" : "+v"(rl0));
;         const int col0 = u.pn * BM + wc * 32 + 8 * fq;
;         int2 sr[2][4];
; #pragma unroll
;         for (int ai = 0; ai < 2; ++ai)
; #pragma unroll
;             for (int m = 0; m < 4; ++m) { const int rl = rl0 + ai * HALF + m * 16;
;                 sr[ai][m] = SLOT[(size_t)u.aux * GCAP_SLOTS + (size_t)u.lt * BM + (rl < u.rows ? rl : 0)]; }
;         __builtin_amdgcn_sched_barrier(0);
; #pragma unroll
;         for (int ai = 0; ai < 2; ++ai)
; #pragma unroll
;             for (int m = 0; m < 4; ++m) { const int rl = rl0 + ai * HALF + m * 16; const bool ok = rl < u.rows;
;                 const int2 s = sr[ai][m]; const float w = __int_as_float(s.y); bf16_t* rowp = YE + (size_t)(ok ? s.x : dummy_row) * 1024 + col0;
; #pragma unroll
;                 for (int bj = 0; bj < 2; ++bj) *(u32x4*)(rowp + bj * HALF) = pack8(acc[ai][bj][m][0] * w, acc[ai][bj][m][1] * w); }
.LBB0_1177:
	s_ashr_i32 s9, s8, 31
	s_lshl_b64 s[8:9], s[8:9], 12
	s_add_u32 s2, s43, s8
	s_addc_u32 s7, s44, s9
	s_lshl_b32 s8, s5, 8
	s_ashr_i32 s9, s8, 31
	s_lshl_b64 s[8:9], s[8:9], 2
	s_add_u32 s2, s2, s8
	s_addc_u32 s5, s7, s9
	s_add_u32 s8, s2, s46
	s_addc_u32 s9, s5, 0
	global_load_dwordx4 v[70:73], v166, s[8:9] offset:16
	global_load_dwordx4 v[78:81], v166, s[8:9]
	global_load_dwordx4 v[66:69], v166, s[8:9] offset:528
	global_load_dwordx4 v[74:77], v166, s[8:9] offset:512
	s_ashr_i32 s5, s4, 31
	v_mov_b32_e32 v164, v167
	s_ashr_i32 s7, s6, 31
	s_lshl_b64 s[4:5], s[4:5], 18
	s_add_u32 s2, s53, s4
	v_add_u32_e32 v160, 32, v164
	s_addc_u32 s8, s56, s5
	s_lshl_b64 s[4:5], s[6:7], 11
	v_cmp_gt_i32_e64 s[18:19], s65, v164
	v_add_u32_e32 v158, 16, v164
	v_cmp_gt_i32_e64 s[12:13], s65, v160
	v_add_u32_e32 v162, 48, v164
	s_add_u32 s68, s2, s4
	v_cndmask_b32_e64 v156, 0, v164, s[18:19]
	v_cmp_gt_i32_e64 s[14:15], s65, v158
	v_cndmask_b32_e64 v160, 0, v160, s[12:13]
	v_cmp_gt_i32_e64 s[10:11], s65, v162
	s_addc_u32 s69, s8, s5
	v_ashrrev_i32_e32 v157, 31, v156
	v_cndmask_b32_e64 v158, 0, v158, s[14:15]
	v_ashrrev_i32_e32 v161, 31, v160
	v_cndmask_b32_e64 v162, 0, v162, s[10:11]
	v_lshl_add_u64 v[156:157], v[156:157], 3, s[68:69]
	v_ashrrev_i32_e32 v159, 31, v158
	v_lshl_add_u64 v[160:161], v[160:161], 3, s[68:69]
	v_ashrrev_i32_e32 v163, 31, v162
	v_lshl_add_u64 v[158:159], v[158:159], 3, s[68:69]
	v_lshl_add_u64 v[162:163], v[162:163], 3, s[68:69]
	s_waitcnt vmcnt(12)
	v_mov_b64_e32 v[172:173], v[220:221]
	v_mov_b64_e32 v[174:175], v[222:223]
	v_mov_b64_e32 v[176:177], v[224:225]
	v_mov_b64_e32 v[178:179], v[226:227]
	v_add_u32_e32 v156, 0x80, v164
	v_add_u32_e32 v160, 0xa0, v164
	v_cmp_gt_i32_e64 s[8:9], s65, v156
	v_add_u32_e32 v158, 0x90, v164
	v_cmp_gt_i32_e64 s[4:5], s65, v160
	v_add_u32_e32 v162, 0xb0, v164
	v_cndmask_b32_e64 v156, 0, v156, s[8:9]
	v_cmp_gt_i32_e64 s[6:7], s65, v158
	v_cndmask_b32_e64 v160, 0, v160, s[4:5]
	v_cmp_gt_i32_e32 vcc, s65, v162
	v_ashrrev_i32_e32 v157, 31, v156
	v_cndmask_b32_e64 v158, 0, v158, s[6:7]
	v_ashrrev_i32_e32 v161, 31, v160
	v_cndmask_b32_e32 v162, 0, v162, vcc
	v_lshl_add_u64 v[156:157], v[156:157], 3, s[68:69]
	v_ashrrev_i32_e32 v159, 31, v158
	v_lshl_add_u64 v[160:161], v[160:161], 3, s[68:69]
	v_ashrrev_i32_e32 v163, 31, v162
	v_lshl_add_u64 v[158:159], v[158:159], 3, s[68:69]
	v_lshl_add_u64 v[180:181], v[162:163], 3, s[68:69]
	v_mov_b64_e32 v[164:165], v[240:241]
	v_mov_b64_e32 v[162:163], v[242:243]
	s_nop 0
	v_mov_b64_e32 v[160:161], v[244:245]
	s_nop 0
	v_mov_b64_e32 v[156:157], v[246:247]
	v_lshl_or_b32 v158, s66, 8, v169
	v_cndmask_b32_e64 v180, v250, v172, s[18:19]
	v_ashrrev_i32_e32 v181, 31, v180
	v_ashrrev_i32_e32 v159, 31, v158
	v_lshlrev_b64 v[180:181], 11, v[180:181]
	v_lshl_add_u64 v[180:181], s[22:23], 0, v[180:181]
	v_lshlrev_b64 v[158:159], 1, v[158:159]
	v_lshl_add_u64 v[180:181], v[180:181], 0, v[158:159]
	v_pk_mul_f32 v[144:145], v[144:145], v[172:173] op_sel:[0,1]
	v_pk_mul_f32 v[142:143], v[142:143], v[172:173] op_sel:[0,1]
	v_pk_mul_f32 v[182:183], v[140:141], v[172:173] op_sel:[0,1]
	v_pk_mul_f32 v[140:141], v[138:139], v[172:173] op_sel:[0,1]
	v_cvt_pk_bf16_f32 v138, v142, v143
	v_cvt_pk_bf16_f32 v139, v144, v145
	v_pk_mul_f32 v[134:135], v[134:135], v[172:173] op_sel:[0,1]
	v_cvt_pk_bf16_f32 v140, v140, v141
	v_cvt_pk_bf16_f32 v141, v182, v183
	s_waitcnt vmcnt(0)
	global_store_dwordx4 v[180:181], v[138:141], off
	v_pk_mul_f32 v[136:137], v[136:137], v[172:173] op_sel:[0,1]
	v_pk_mul_f32 v[128:129], v[128:129], v[174:175] op_sel:[0,1]
	v_pk_mul_f32 v[138:139], v[132:133], v[172:173] op_sel:[0,1]
	v_pk_mul_f32 v[132:133], v[130:131], v[172:173] op_sel:[0,1]
	v_cvt_pk_bf16_f32 v130, v134, v135
	v_cvt_pk_bf16_f32 v131, v136, v137
	v_pk_mul_f32 v[126:127], v[126:127], v[174:175] op_sel:[0,1]
	v_cvt_pk_bf16_f32 v132, v132, v133
	v_cvt_pk_bf16_f32 v133, v138, v139
	global_store_dwordx4 v[180:181], v[130:133], off offset:256
	v_pk_mul_f32 v[118:119], v[118:119], v[174:175] op_sel:[0,1]
	v_pk_mul_f32 v[120:121], v[120:121], v[174:175] op_sel:[0,1]
	v_cndmask_b32_e64 v130, v250, v174, s[14:15]
	v_ashrrev_i32_e32 v131, 31, v130
	v_lshlrev_b64 v[130:131], 11, v[130:131]
	v_lshl_add_u64 v[130:131], s[22:23], 0, v[130:131]
	v_lshl_add_u64 v[130:131], v[130:131], 0, v[158:159]
	v_pk_mul_f32 v[132:133], v[124:125], v[174:175] op_sel:[0,1]
	v_pk_mul_f32 v[124:125], v[122:123], v[174:175] op_sel:[0,1]
	v_cvt_pk_bf16_f32 v122, v126, v127
	v_cvt_pk_bf16_f32 v123, v128, v129
	v_pk_mul_f32 v[112:113], v[112:113], v[176:177] op_sel:[0,1]
	v_cvt_pk_bf16_f32 v124, v124, v125
	v_cvt_pk_bf16_f32 v125, v132, v133
	global_store_dwordx4 v[130:131], v[122:125], off
	v_pk_mul_f32 v[110:111], v[110:111], v[176:177] op_sel:[0,1]
	v_pk_mul_f32 v[102:103], v[102:103], v[176:177] op_sel:[0,1]
	v_pk_mul_f32 v[122:123], v[116:117], v[174:175] op_sel:[0,1]
	v_pk_mul_f32 v[116:117], v[114:115], v[174:175] op_sel:[0,1]
	v_cvt_pk_bf16_f32 v114, v118, v119
	v_cvt_pk_bf16_f32 v115, v120, v121
	v_pk_mul_f32 v[104:105], v[104:105], v[176:177] op_sel:[0,1]
	v_cvt_pk_bf16_f32 v116, v116, v117
	v_cvt_pk_bf16_f32 v117, v122, v123
	global_store_dwordx4 v[130:131], v[114:117], off offset:256
	v_pk_mul_f32 v[96:97], v[96:97], v[178:179] op_sel:[0,1]
	v_pk_mul_f32 v[94:95], v[94:95], v[178:179] op_sel:[0,1]
	v_cndmask_b32_e64 v114, v250, v176, s[12:13]
	v_ashrrev_i32_e32 v115, 31, v114
	v_lshlrev_b64 v[114:115], 11, v[114:115]
	v_lshl_add_u64 v[114:115], s[22:23], 0, v[114:115]
	v_lshl_add_u64 v[114:115], v[114:115], 0, v[158:159]
	v_pk_mul_f32 v[116:117], v[108:109], v[176:177] op_sel:[0,1]
; __device__ __forceinline__ u32x4 pack8(const f32x4 v0, const f32x4 v1) { u32x4 w; w.x = cvt_pk_bf16(v0[0], v0[1]); w.y = cvt_pk_bf16(v0[2], v0[3]); w.z = cvt_pk_bf16(v1[0], v1[1]); w.w = cvt_pk_bf16(v1[2], v1[3]); return w; }
; #define PG8_BAR __builtin_amdgcn_s_barrier()
;     __device__ __forceinline__ void operator()(const f32x4 (&acc)[2][2][4][2], const Unit& u, int wr, int wc, int fr, int fq) const {
;     ...
; #pragma unroll
;         for (int ai = 0; ai < 2; ++ai)
; #pragma unroll
;             for (int m = 0; m < 4; ++m) { const int rl = rl0 + ai * HALF + m * 16; const bool ok = rl < u.rows;
;                 const int2 s = sr[ai][m]; const float w = __int_as_float(s.y); bf16_t* rowp = YE + (size_t)(ok ? s.x : dummy_row) * 1024 + col0;
; #pragma unroll
;                 for (int bj = 0; bj < 2; ++bj) *(u32x4*)(rowp + bj * HALF) = pack8(acc[ai][bj][m][0] * w, acc[ai][bj][m][1] * w); }
; template <class Epi, class Sched, bool ALIGN_EPI = false, bool SP2 = false, bool GATHER = false>
; __device__ __forceinline__ void gemm_phase(PG8_LAS unsigned char* lds, const Gemm g, const Sched& S, const Epi& E, const int2* gslot = nullptr, PG8_LAS unsigned char* gtab = nullptr) {
;     ...
;         if constexpr (!Epi::AFTER_DRAIN) { E(acc, cur, wr, wc, fr, fq); S.done(cur); }
;         if (!has_next) break;
;         E.init(acc, pre);
;         cur = nxt; cA = nA; cB = nB; ++ui;
;         if constexpr (GATHER) { _Pragma("unroll") for (int h_ = 0; h_ < 2; ++h_) _Pragma("unroll") for (int i_ = 0; i_ < 2; ++i_) vC[h_][i_] = vN[h_][i_]; }
;         if constexpr (ALIGN_EPI) { if (wr == 1) PG8_BAR; }
	v_pk_mul_f32 v[108:109], v[106:107], v[176:177] op_sel:[0,1]
	v_cvt_pk_bf16_f32 v106, v110, v111
	v_cvt_pk_bf16_f32 v107, v112, v113
	v_pk_mul_f32 v[86:87], v[86:87], v[178:179] op_sel:[0,1]
	v_cvt_pk_bf16_f32 v108, v108, v109
	v_cvt_pk_bf16_f32 v109, v116, v117
	global_store_dwordx4 v[114:115], v[106:109], off
	v_pk_mul_f32 v[88:89], v[88:89], v[178:179] op_sel:[0,1]
	v_pk_mul_f32 v[64:65], v[64:65], v[164:165] op_sel:[0,1]
	v_pk_mul_f32 v[106:107], v[100:101], v[176:177] op_sel:[0,1]
	v_pk_mul_f32 v[100:101], v[98:99], v[176:177] op_sel:[0,1]
	v_cvt_pk_bf16_f32 v98, v102, v103
	v_cvt_pk_bf16_f32 v99, v104, v105
	v_pk_mul_f32 v[62:63], v[62:63], v[164:165] op_sel:[0,1]
	v_cvt_pk_bf16_f32 v100, v100, v101
	v_cvt_pk_bf16_f32 v101, v106, v107
	global_store_dwordx4 v[114:115], v[98:101], off offset:256
	v_pk_mul_f32 v[54:55], v[54:55], v[164:165] op_sel:[0,1]
	v_pk_mul_f32 v[56:57], v[56:57], v[164:165] op_sel:[0,1]
	v_cndmask_b32_e64 v98, v250, v178, s[10:11]
	v_ashrrev_i32_e32 v99, 31, v98
	v_lshlrev_b64 v[98:99], 11, v[98:99]
	v_lshl_add_u64 v[98:99], s[22:23], 0, v[98:99]
	v_lshl_add_u64 v[98:99], v[98:99], 0, v[158:159]
	v_pk_mul_f32 v[100:101], v[92:93], v[178:179] op_sel:[0,1]
	v_pk_mul_f32 v[92:93], v[90:91], v[178:179] op_sel:[0,1]
	v_cvt_pk_bf16_f32 v90, v94, v95
	v_cvt_pk_bf16_f32 v91, v96, v97
	v_pk_mul_f32 v[48:49], v[48:49], v[162:163] op_sel:[0,1]
	v_cvt_pk_bf16_f32 v92, v92, v93
	v_cvt_pk_bf16_f32 v93, v100, v101
	global_store_dwordx4 v[98:99], v[90:93], off
	v_pk_mul_f32 v[46:47], v[46:47], v[162:163] op_sel:[0,1]
	v_pk_mul_f32 v[38:39], v[38:39], v[162:163] op_sel:[0,1]
	v_pk_mul_f32 v[90:91], v[84:85], v[178:179] op_sel:[0,1]
	v_pk_mul_f32 v[84:85], v[82:83], v[178:179] op_sel:[0,1]
	v_cvt_pk_bf16_f32 v82, v86, v87
	v_cvt_pk_bf16_f32 v83, v88, v89
	v_pk_mul_f32 v[40:41], v[40:41], v[162:163] op_sel:[0,1]
	v_cvt_pk_bf16_f32 v84, v84, v85
	v_cvt_pk_bf16_f32 v85, v90, v91
	global_store_dwordx4 v[98:99], v[82:85], off offset:256
	v_pk_mul_f32 v[32:33], v[32:33], v[160:161] op_sel:[0,1]
	v_pk_mul_f32 v[30:31], v[30:31], v[160:161] op_sel:[0,1]
	v_cndmask_b32_e64 v82, v250, v164, s[8:9]
	v_ashrrev_i32_e32 v83, 31, v82
	v_lshlrev_b64 v[82:83], 11, v[82:83]
	v_lshl_add_u64 v[82:83], s[22:23], 0, v[82:83]
	v_lshl_add_u64 v[82:83], v[82:83], 0, v[158:159]
	v_pk_mul_f32 v[84:85], v[60:61], v[164:165] op_sel:[0,1]
	v_pk_mul_f32 v[60:61], v[58:59], v[164:165] op_sel:[0,1]
	v_cvt_pk_bf16_f32 v58, v62, v63
	v_cvt_pk_bf16_f32 v59, v64, v65
	v_pk_mul_f32 v[22:23], v[22:23], v[160:161] op_sel:[0,1]
	v_cvt_pk_bf16_f32 v60, v60, v61
	v_cvt_pk_bf16_f32 v61, v84, v85
	global_store_dwordx4 v[82:83], v[58:61], off
	v_pk_mul_f32 v[24:25], v[24:25], v[160:161] op_sel:[0,1]
	v_pk_mul_f32 v[16:17], v[16:17], v[156:157] op_sel:[0,1]
	v_pk_mul_f32 v[58:59], v[52:53], v[164:165] op_sel:[0,1]
	v_pk_mul_f32 v[52:53], v[50:51], v[164:165] op_sel:[0,1]
	v_cvt_pk_bf16_f32 v50, v54, v55
	v_cvt_pk_bf16_f32 v51, v56, v57
	v_pk_mul_f32 v[14:15], v[14:15], v[156:157] op_sel:[0,1]
	v_cvt_pk_bf16_f32 v52, v52, v53
	v_cvt_pk_bf16_f32 v53, v58, v59
	global_store_dwordx4 v[82:83], v[50:53], off offset:256
	v_pk_mul_f32 v[8:9], v[8:9], v[156:157] op_sel:[0,1]
	v_pk_mul_f32 v[6:7], v[6:7], v[156:157] op_sel:[0,1]
	v_cndmask_b32_e64 v50, v250, v162, s[6:7]
	v_ashrrev_i32_e32 v51, 31, v50
	v_lshlrev_b64 v[50:51], 11, v[50:51]
	v_lshl_add_u64 v[50:51], s[22:23], 0, v[50:51]
	v_lshl_add_u64 v[50:51], v[50:51], 0, v[158:159]
	v_pk_mul_f32 v[52:53], v[44:45], v[162:163] op_sel:[0,1]
	v_pk_mul_f32 v[44:45], v[42:43], v[162:163] op_sel:[0,1]
	v_cvt_pk_bf16_f32 v42, v46, v47
	v_cvt_pk_bf16_f32 v43, v48, v49
	s_nop 0
	v_cvt_pk_bf16_f32 v44, v44, v45
	v_cvt_pk_bf16_f32 v45, v52, v53
	global_store_dwordx4 v[50:51], v[42:45], off
	s_nop 1
	v_pk_mul_f32 v[42:43], v[36:37], v[162:163] op_sel:[0,1]
	v_pk_mul_f32 v[36:37], v[34:35], v[162:163] op_sel:[0,1]
	v_cvt_pk_bf16_f32 v34, v38, v39
	v_cvt_pk_bf16_f32 v35, v40, v41
	s_nop 0
	v_cvt_pk_bf16_f32 v36, v36, v37
	v_cvt_pk_bf16_f32 v37, v42, v43
	global_store_dwordx4 v[50:51], v[34:37], off offset:256
	s_nop 1
	v_cndmask_b32_e64 v34, v250, v160, s[4:5]
	v_ashrrev_i32_e32 v35, 31, v34
	v_lshlrev_b64 v[34:35], 11, v[34:35]
	v_lshl_add_u64 v[34:35], s[22:23], 0, v[34:35]
	v_lshl_add_u64 v[34:35], v[34:35], 0, v[158:159]
	v_pk_mul_f32 v[36:37], v[28:29], v[160:161] op_sel:[0,1]
	v_pk_mul_f32 v[28:29], v[26:27], v[160:161] op_sel:[0,1]
	v_cvt_pk_bf16_f32 v26, v30, v31
	v_cvt_pk_bf16_f32 v27, v32, v33
	s_mov_b64 s[4:5], -1
	v_cvt_pk_bf16_f32 v28, v28, v29
	v_cvt_pk_bf16_f32 v29, v36, v37
	global_store_dwordx4 v[34:35], v[26:29], off
	s_nop 1
	v_pk_mul_f32 v[26:27], v[20:21], v[160:161] op_sel:[0,1]
	v_pk_mul_f32 v[20:21], v[18:19], v[160:161] op_sel:[0,1]
	v_cvt_pk_bf16_f32 v18, v22, v23
	v_cvt_pk_bf16_f32 v19, v24, v25
	s_nop 0
	v_cvt_pk_bf16_f32 v20, v20, v21
	v_cvt_pk_bf16_f32 v21, v26, v27
	global_store_dwordx4 v[34:35], v[18:21], off offset:256
	s_nop 1
	v_cndmask_b32_e32 v18, v250, v156, vcc
	v_ashrrev_i32_e32 v19, 31, v18
	v_lshlrev_b64 v[18:19], 11, v[18:19]
	v_lshl_add_u64 v[18:19], s[22:23], 0, v[18:19]
	v_lshl_add_u64 v[18:19], v[18:19], 0, v[158:159]
	v_pk_mul_f32 v[20:21], v[12:13], v[156:157] op_sel:[0,1]
	v_pk_mul_f32 v[12:13], v[10:11], v[156:157] op_sel:[0,1]
	v_cvt_pk_bf16_f32 v10, v14, v15
	v_cvt_pk_bf16_f32 v11, v16, v17
	s_andn2_b64 vcc, exec, s[30:31]
	v_cvt_pk_bf16_f32 v12, v12, v13
	v_cvt_pk_bf16_f32 v13, v20, v21
	global_store_dwordx4 v[18:19], v[10:13], off
	s_nop 1
	v_pk_mul_f32 v[10:11], v[4:5], v[156:157] op_sel:[0,1]
	v_pk_mul_f32 v[4:5], v[2:3], v[156:157] op_sel:[0,1]
	v_cvt_pk_bf16_f32 v2, v6, v7
	v_cvt_pk_bf16_f32 v3, v8, v9
	s_nop 0
	v_cvt_pk_bf16_f32 v4, v4, v5
	v_cvt_pk_bf16_f32 v5, v10, v11
	global_store_dwordx4 v[18:19], v[2:5], off offset:256
	s_cbranch_vccnz .LBB0_1166
	s_andn2_b64 vcc, exec, s[20:21]
	s_cbranch_vccnz .LBB0_1165
	s_barrier
	s_branch .LBB0_1165

; __device__ __forceinline__ float wave_sum(float v) { v = half_sum32(v); float a; const float b = swap32_other(v, a); return a + b; }
; __device__ __forceinline__ void ln_apply(f32x4 (&v)[4], const float* g, const float* b, int lane) {
;     ...
;     for (int j = 0; j < 4; ++j) s += (v[j].x + v[j].y) + (v[j].z + v[j].w);
;     const float mean = wave_sum(s) * (1.f / D); float s2 = 0.f;
; __device__ __forceinline__ void combine_ln_phase(Frame& F, const bf16* YE, const float* g, const float* b, float* X, bf16* XB) { LTID();
;     ...
;         for (int j = 0; j < 4; ++j) { const v2u w = xw[j]; v[j] = (f32x4){bflo(w.x), bfhi(w.x), bflo(w.y), bfhi(w.y)} * DN_ALPHA; }
; #pragma unroll
;         for (int k = 0; k < 4; ++k) {
; #pragma unroll
;             for (int j = 0; j < 4; ++j) { const v2u w = yw[k][j]; v[j].x += bflo(w.x); v[j].y += bfhi(w.x); v[j].z += bflo(w.y); v[j].w += bfhi(w.y); } }
.LBB0_1237:
	v_lshlrev_b32_e32 v92, 16, v90
	v_and_b32_e32 v93, 0xffff0000, v90
	v_lshlrev_b32_e32 v90, 16, v91
	v_and_b32_e32 v91, 0xffff0000, v91
	v_lshlrev_b32_e32 v98, 16, v78
	v_and_b32_e32 v99, 0xffff0000, v78
	v_lshlrev_b32_e32 v100, 16, v79
	v_and_b32_e32 v101, 0xffff0000, v79
	v_lshlrev_b32_e32 v78, 16, v80
	v_and_b32_e32 v79, 0xffff0000, v80
	v_lshlrev_b32_e32 v80, 16, v81
	v_and_b32_e32 v81, 0xffff0000, v81
	v_pk_fma_f32 v[78:79], v[92:93], s[86:87], v[78:79] op_sel_hi:[1,0,1]
	v_lshlrev_b32_e32 v92, 16, v76
	v_and_b32_e32 v93, 0xffff0000, v76
	v_pk_fma_f32 v[80:81], v[90:91], s[86:87], v[80:81] op_sel_hi:[1,0,1]
	v_lshlrev_b32_e32 v76, 16, v77
	v_and_b32_e32 v77, 0xffff0000, v77
	v_pk_add_f32 v[76:77], v[80:81], v[76:77]
	v_lshlrev_b32_e32 v80, 16, v83
	v_and_b32_e32 v81, 0xffff0000, v83
	v_pk_add_f32 v[76:77], v[76:77], v[80:81]
	v_lshlrev_b32_e32 v80, 16, v89
	v_and_b32_e32 v81, 0xffff0000, v89
	v_lshlrev_b32_e32 v94, 16, v86
	v_and_b32_e32 v95, 0xffff0000, v86
	v_lshlrev_b32_e32 v86, 16, v87
	v_and_b32_e32 v87, 0xffff0000, v87
	v_pk_add_f32 v[80:81], v[76:77], v[80:81]
	v_lshlrev_b32_e32 v76, 16, v72
	v_and_b32_e32 v77, 0xffff0000, v72
	v_lshlrev_b32_e32 v72, 16, v73
	v_and_b32_e32 v73, 0xffff0000, v73
	v_pk_add_f32 v[78:79], v[78:79], v[92:93]
	v_lshlrev_b32_e32 v92, 16, v82
	v_and_b32_e32 v93, 0xffff0000, v82
	v_pk_fma_f32 v[76:77], v[94:95], s[86:87], v[76:77] op_sel_hi:[1,0,1]
	v_lshlrev_b32_e32 v82, 16, v68
	v_and_b32_e32 v83, 0xffff0000, v68
	v_pk_fma_f32 v[72:73], v[86:87], s[86:87], v[72:73] op_sel_hi:[1,0,1]
	v_lshlrev_b32_e32 v68, 16, v69
	v_and_b32_e32 v69, 0xffff0000, v69
	v_pk_add_f32 v[76:77], v[76:77], v[82:83]
	v_lshlrev_b32_e32 v82, 16, v70
	v_and_b32_e32 v83, 0xffff0000, v70
	v_pk_add_f32 v[68:69], v[72:73], v[68:69]
	v_lshlrev_b32_e32 v70, 16, v71
	v_and_b32_e32 v71, 0xffff0000, v71
	v_pk_add_f32 v[68:69], v[68:69], v[70:71]
	v_lshlrev_b32_e32 v70, 16, v75
	v_and_b32_e32 v71, 0xffff0000, v75
	v_lshlrev_b32_e32 v96, 16, v84
	v_and_b32_e32 v97, 0xffff0000, v84
	v_lshlrev_b32_e32 v84, 16, v85
	v_and_b32_e32 v85, 0xffff0000, v85
	v_pk_add_f32 v[72:73], v[68:69], v[70:71]
	v_lshlrev_b32_e32 v68, 16, v14
	v_and_b32_e32 v69, 0xffff0000, v14
	v_lshlrev_b32_e32 v14, 16, v15
	v_and_b32_e32 v15, 0xffff0000, v15
	v_pk_fma_f32 v[68:69], v[96:97], s[86:87], v[68:69] op_sel_hi:[1,0,1]
	v_lshlrev_b32_e32 v70, 16, v10
	v_and_b32_e32 v71, 0xffff0000, v10
	v_pk_fma_f32 v[14:15], v[84:85], s[86:87], v[14:15] op_sel_hi:[1,0,1]
	v_lshlrev_b32_e32 v10, 16, v11
	v_and_b32_e32 v11, 0xffff0000, v11
	v_pk_add_f32 v[68:69], v[68:69], v[70:71]
	v_lshlrev_b32_e32 v70, 16, v12
	v_and_b32_e32 v71, 0xffff0000, v12
	v_pk_add_f32 v[10:11], v[14:15], v[10:11]
	v_lshlrev_b32_e32 v12, 16, v13
	v_and_b32_e32 v13, 0xffff0000, v13
	v_pk_add_f32 v[10:11], v[10:11], v[12:13]
	v_lshlrev_b32_e32 v12, 16, v17
	v_and_b32_e32 v13, 0xffff0000, v17
	v_pk_add_f32 v[10:11], v[10:11], v[12:13]
	v_lshlrev_b32_e32 v12, 16, v6
	v_and_b32_e32 v13, 0xffff0000, v6
	v_lshlrev_b32_e32 v6, 16, v7
	v_and_b32_e32 v7, 0xffff0000, v7
	v_pk_fma_f32 v[12:13], v[98:99], s[86:87], v[12:13] op_sel_hi:[1,0,1]
	v_lshlrev_b32_e32 v14, 16, v2
	v_and_b32_e32 v15, 0xffff0000, v2
	v_pk_fma_f32 v[6:7], v[100:101], s[86:87], v[6:7] op_sel_hi:[1,0,1]
	v_lshlrev_b32_e32 v2, 16, v3
	v_and_b32_e32 v3, 0xffff0000, v3
	v_pk_add_f32 v[12:13], v[12:13], v[14:15]
	v_lshlrev_b32_e32 v14, 16, v4
	v_and_b32_e32 v15, 0xffff0000, v4
	v_pk_add_f32 v[2:3], v[6:7], v[2:3]
	v_lshlrev_b32_e32 v4, 16, v5
	v_and_b32_e32 v5, 0xffff0000, v5
	v_pk_add_f32 v[12:13], v[12:13], v[14:15]
	v_lshlrev_b32_e32 v14, 16, v8
	v_and_b32_e32 v15, 0xffff0000, v8
	v_pk_add_f32 v[2:3], v[2:3], v[4:5]
	v_lshlrev_b32_e32 v4, 16, v9
	v_and_b32_e32 v5, 0xffff0000, v9
	v_pk_add_f32 v[78:79], v[78:79], v[92:93]
	v_lshlrev_b32_e32 v92, 16, v88
	v_and_b32_e32 v93, 0xffff0000, v88
	v_pk_add_f32 v[76:77], v[76:77], v[82:83]
	v_lshlrev_b32_e32 v82, 16, v74
	v_and_b32_e32 v83, 0xffff0000, v74
	v_pk_add_f32 v[68:69], v[68:69], v[70:71]
	v_lshlrev_b32_e32 v70, 16, v16
	v_and_b32_e32 v71, 0xffff0000, v16
	v_pk_add_f32 v[14:15], v[12:13], v[14:15]
	v_pk_add_f32 v[16:17], v[2:3], v[4:5]
	v_pk_add_f32 v[78:79], v[78:79], v[92:93]
	v_pk_add_f32 v[76:77], v[76:77], v[82:83]
	v_pk_add_f32 v[70:71], v[68:69], v[70:71]
	v_add_f32_e32 v2, v80, v81
	v_add_f32_e32 v3, v78, v79
	v_add_f32_e32 v2, v3, v2
	v_add_f32_e32 v3, v72, v73
	v_add_f32_e32 v4, v76, v77
	v_add_f32_e32 v2, 0, v2
	v_add_f32_e32 v3, v4, v3
	v_add_f32_e32 v2, v3, v2
	v_add_f32_e32 v3, v10, v11
	v_add_f32_e32 v4, v70, v71
	v_add_f32_e32 v3, v4, v3
	v_add_f32_e32 v2, v3, v2
	v_add_f32_e32 v3, v16, v17
	v_add_f32_e32 v4, v14, v15
	v_add_f32_e32 v3, v4, v3
	v_add_f32_e32 v2, v3, v2
	s_nop 1
	v_add_f32_dpp v2, v2, v2 quad_perm:[1,0,3,2] row_mask:0xf bank_mask:0xf bound_ctrl:1
	s_nop 1
	v_add_f32_dpp v2, v2, v2 quad_perm:[2,3,0,1] row_mask:0xf bank_mask:0xf bound_ctrl:1
; __device__ __forceinline__ float wave_sum(float v) { v = half_sum32(v); float a; const float b = swap32_other(v, a); return a + b; }
; #define GAS __attribute__((address_space(1)))
; __device__ __forceinline__ unsigned pk2(float lo, float hi) { f32x2_t v = {lo, hi}; bf16x2_t b = __builtin_convertvector(v, bf16x2_t); return __builtin_bit_cast(unsigned, b); }
; __device__ __forceinline__ void ln_apply(f32x4 (&v)[4], const float* g, const float* b, int lane) {
;     ...
;     const float mean = wave_sum(s) * (1.f / D); float s2 = 0.f;
; #pragma unroll
;     for (int j = 0; j < 4; ++j) { v[j] = v[j] - mean; s2 += (v[j].x * v[j].x + v[j].y * v[j].y) + (v[j].z * v[j].z + v[j].w * v[j].w); }
;     const float rstd = 1.f / sqrtf(wave_sum(s2) * (1.f / D) + LN_EPS);
; #pragma unroll
;     for (int j = 0; j < 4; ++j) { const f32x4 gg = *((const GAS f32x4*)g + lane + 64 * j), bb = *((const GAS f32x4*)b + lane + 64 * j); v[j] = v[j] * rstd * gg + bb; }
; }
; __device__ __forceinline__ void store_x(const f32x4 (&v)[4], float* X, bf16* XB, size_t row, int lane) {
;     GAS v2u* bo = (GAS v2u*)(XB + row * D) + lane;
; #pragma unroll
;     for (int j = 0; j < 4; ++j) { v2u w; w.x = pk2(v[j].x, v[j].y); w.y = pk2(v[j].z, v[j].w); bo[64 * j] = w; }
;     if (X) { GAS f32x4* xo = (GAS f32x4*)(X + row * D) + lane;
; #pragma unroll
;         for (int j = 0; j < 4; ++j) __builtin_nontemporal_store(v[j], xo + 64 * j); }
	s_nop 1
	v_add_f32_dpp v2, v2, v2 row_half_mirror row_mask:0xf bank_mask:0xf bound_ctrl:1
	s_nop 1
	v_add_f32_dpp v2, v2, v2 row_mirror row_mask:0xf bank_mask:0xf bound_ctrl:1
	v_mov_b32_e32 v3, v2
	s_nop 1
	v_permlane16_swap_b32 v3, v2
	s_nop 0
	v_add_f32_e32 v2, v2, v3
	v_mov_b32_e32 v3, v2
	s_nop 1
	v_permlane32_swap_b32 v3, v2
	s_nop 0
	v_add_f32_e32 v2, v2, v3
	v_fmac_f32_e32 v81, 0xba800000, v2
	v_fmac_f32_e32 v79, 0xba800000, v2
	v_fmamk_f32 v80, v2, 0xba800000, v80
	v_fmamk_f32 v78, v2, 0xba800000, v78
	v_mul_f32_e32 v3, v79, v79
	v_mul_f32_e32 v4, v81, v81
	v_fmac_f32_e32 v3, v78, v78
	v_fmac_f32_e32 v4, v80, v80
	v_fmac_f32_e32 v73, 0xba800000, v2
	v_fmac_f32_e32 v77, 0xba800000, v2
	v_add_f32_e32 v3, v3, v4
	v_fmamk_f32 v72, v2, 0xba800000, v72
	v_fmamk_f32 v76, v2, 0xba800000, v76
	v_mul_f32_e32 v4, v77, v77
	v_mul_f32_e32 v5, v73, v73
	v_fmac_f32_e32 v4, v76, v76
	v_fmac_f32_e32 v5, v72, v72
	v_add_f32_e32 v4, v4, v5
	v_fmac_f32_e32 v11, 0xba800000, v2
	v_fmac_f32_e32 v71, 0xba800000, v2
	v_add_f32_e32 v3, v3, v4
	v_fmamk_f32 v10, v2, 0xba800000, v10
	v_fmamk_f32 v70, v2, 0xba800000, v70
	v_mul_f32_e32 v4, v71, v71
	v_mul_f32_e32 v5, v11, v11
	v_fmac_f32_e32 v4, v70, v70
	v_fmac_f32_e32 v5, v10, v10
	v_add_f32_e32 v4, v4, v5
	v_fmac_f32_e32 v17, 0xba800000, v2
	v_fmac_f32_e32 v15, 0xba800000, v2
	v_add_f32_e32 v3, v4, v3
	v_fmamk_f32 v16, v2, 0xba800000, v16
	v_fmamk_f32 v14, v2, 0xba800000, v14
	v_mul_f32_e32 v2, v15, v15
	v_mul_f32_e32 v4, v17, v17
	v_fmac_f32_e32 v2, v14, v14
	v_fmac_f32_e32 v4, v16, v16
	v_add_f32_e32 v2, v2, v4
	v_add_f32_e32 v2, v2, v3
	s_nop 1
	v_add_f32_dpp v2, v2, v2 quad_perm:[1,0,3,2] row_mask:0xf bank_mask:0xf bound_ctrl:1
	s_nop 1
	v_add_f32_dpp v2, v2, v2 quad_perm:[2,3,0,1] row_mask:0xf bank_mask:0xf bound_ctrl:1
	s_nop 1
	v_add_f32_dpp v2, v2, v2 row_half_mirror row_mask:0xf bank_mask:0xf bound_ctrl:1
	s_nop 1
	v_add_f32_dpp v2, v2, v2 row_mirror row_mask:0xf bank_mask:0xf bound_ctrl:1
	v_mov_b32_e32 v3, v2
	s_nop 1
	v_permlane16_swap_b32 v3, v2
	s_nop 0
	v_add_f32_e32 v2, v2, v3
	v_mov_b32_e32 v3, v2
	s_nop 1
	v_permlane32_swap_b32 v3, v2
	s_nop 0
	v_add_f32_e32 v2, v2, v3
	v_fmamk_f32 v2, v2, 0x3a800000, v228
	v_cmp_gt_f32_e32 vcc, s3, v2
	v_mul_f32_e32 v3, 0x4f800000, v2
	s_nop 0
	v_cndmask_b32_e32 v2, v2, v3, vcc
	v_sqrt_f32_e32 v3, v2
	s_nop 0
	v_add_u32_e32 v4, -1, v3
	v_fma_f32 v5, -v4, v3, v2
	v_cmp_ge_f32_e64 s[4:5], 0, v5
	v_add_u32_e32 v5, 1, v3
	s_nop 0
	v_cndmask_b32_e64 v4, v3, v4, s[4:5]
	v_fma_f32 v3, -v5, v3, v2
	v_cmp_lt_f32_e64 s[4:5], 0, v3
	s_nop 1
	v_cndmask_b32_e64 v3, v4, v5, s[4:5]
	v_mul_f32_e32 v4, 0x37800000, v3
	v_cndmask_b32_e32 v3, v3, v4, vcc
	v_cmp_class_f32_e32 vcc, v2, v229
	s_nop 1
	v_cndmask_b32_e32 v2, v3, v2, vcc
	v_div_scale_f32 v3, s[4:5], v2, v2, 1.0
	v_rcp_f32_e32 v4, v3
	s_nop 0
	v_fma_f32 v5, -v3, v4, 1.0
	v_fmac_f32_e32 v4, v5, v4
	v_div_scale_f32 v5, vcc, 1.0, v2, 1.0
	v_mul_f32_e32 v6, v5, v4
	v_fma_f32 v7, -v3, v6, v5
	v_fmac_f32_e32 v6, v7, v4
	v_fma_f32 v3, -v3, v6, v5
	v_div_fmas_f32 v3, v3, v4, v6
	v_div_fixup_f32 v68, v3, v2, 1.0
	v_pk_mul_f32 v[12:13], v[78:79], v[68:69] op_sel_hi:[1,0]
	v_pk_mul_f32 v[74:75], v[80:81], v[68:69] op_sel_hi:[1,0]
	v_pk_mul_f32 v[72:73], v[72:73], v[68:69] op_sel_hi:[1,0]
	v_pk_mul_f32 v[70:71], v[70:71], v[68:69] op_sel_hi:[1,0]
	v_pk_mul_f32 v[10:11], v[10:11], v[68:69] op_sel_hi:[1,0]
	v_pk_mul_f32 v[14:15], v[14:15], v[68:69] op_sel_hi:[1,0]
	v_pk_mul_f32 v[16:17], v[16:17], v[68:69] op_sel_hi:[1,0]
	s_andn2_b64 vcc, exec, s[8:9]
	s_waitcnt vmcnt(20)
	v_pk_fma_f32 v[4:5], v[112:113], v[74:75], v[128:129]
	v_pk_fma_f32 v[2:3], v[110:111], v[12:13], v[126:127]
	v_pk_mul_f32 v[12:13], v[76:77], v[68:69] op_sel_hi:[1,0]
	v_cvt_pk_bf16_f32 v68, v2, v3
	v_cvt_pk_bf16_f32 v69, v4, v5
	v_pk_fma_f32 v[8:9], v[116:117], v[72:73], v[132:133]
	v_pk_fma_f32 v[6:7], v[114:115], v[12:13], v[130:131]
	v_pk_fma_f32 v[12:13], v[120:121], v[10:11], v[136:137]
	v_pk_fma_f32 v[10:11], v[118:119], v[70:71], v[134:135]
	v_pk_fma_f32 v[16:17], v[124:125], v[16:17], v[140:141]
	s_waitcnt vmcnt(0)
	global_store_dwordx2 v[24:25], v[68:69], off offset:-1024
	v_cvt_pk_bf16_f32 v68, v6, v7
	v_cvt_pk_bf16_f32 v69, v8, v9
	v_pk_fma_f32 v[14:15], v[122:123], v[14:15], v[138:139]
	global_store_dwordx2 v[24:25], v[68:69], off offset:-512
	v_cvt_pk_bf16_f32 v68, v10, v11
	v_cvt_pk_bf16_f32 v69, v12, v13
	global_store_dwordx2 v[24:25], v[68:69], off
	v_cvt_pk_bf16_f32 v68, v14, v15
	v_cvt_pk_bf16_f32 v69, v16, v17
	global_store_dwordx2 v[24:25], v[68:69], off offset:512
	s_cbranch_vccnz .LBB0_1234
	global_store_dwordx4 v[26:27], v[2:5], off offset:-2048 nt
	global_store_dwordx4 v[26:27], v[6:9], off offset:-1024 nt
	global_store_dwordx4 v[26:27], v[10:13], off nt
	global_store_dwordx4 v[26:27], v[14:17], off offset:1024 nt
	s_branch .LBB0_1234
